# attention unit end: the barrier that frees the LDS ring for the next unit waits lgkmcnt(0) only (the unit's output stores no longer drain before the next unit's loads are issued)
# baseline (speedup 1.0000x reference)
; template <class Mid> __device__ __forceinline__ void attn_unit(const Mid& mid, LAS unsigned char* lds, const bf16* __restrict__ Qu, const bf16* __restrict__ Kh, const bf16* __restrict__ Vh, int q0, int NT, ...
;     ...
;     asm volatile("s_waitcnt vmcnt(0) lgkmcnt(0)\n\ts_barrier" ::: "memory");
; __global__ void __launch_bounds__(NTHR, 2) mk_fwd(Args args) {
;     ...
;                 for (int u = vcu; u < nunits; u += G) {
.LBB0_446:
	s_waitcnt lgkmcnt(0)
	s_barrier
	s_add_i32 s54, s6, s54
	s_add_i32 s55, s55, s64
	s_cmpk_gt_i32 s55, 0x87f
	s_cbranch_scc1 .LBB0_476

; template <class Mid> __device__ __forceinline__ void attn_unit(const Mid& mid, LAS unsigned char* lds, const bf16* __restrict__ Qu, const bf16* __restrict__ Kh, const bf16* __restrict__ Vh, int q0, int NT, ...
;     ...
;     asm volatile("s_waitcnt vmcnt(0) lgkmcnt(0)\n\ts_barrier" ::: "memory");
; __global__ void __launch_bounds__(NTHR, 2) mk_fwd(Args args) {
;     ...
;                 for (int u = vcu; u < nunits; u += G) {
.LBB0_1351:
	s_waitcnt lgkmcnt(0)
	s_barrier
	s_add_i32 s48, s4, s48
	s_add_i32 s49, s49, s64
	s_cmpk_gt_i32 s49, 0x7ff
	s_cbranch_scc1 .LBB0_1373
